# P8 gate|up epilogue: regenerated fast path for the cached-row-scale case (8 scales read together, packed fma/mul around exp/rcp, running store address), same f32 math
# speedup vs baseline: 1.0102x; 1.0102x over previous
.LBB0_1750:
	s_lshl_b32 s15, s15, 8
	s_andn2_b64 vcc, exec, s[26:27]
	v_lshl_add_u32 v176, s15, 2, v171
	s_cbranch_vccnz .LBB0_1752
	s_branch .Lp8fast

.Lp8_tail:
	s_cbranch_vccnz .LBB0_1737
	s_andn2_b64 vcc, exec, s[0:1]
	s_cbranch_vccnz .LBB0_1736
	s_barrier
	s_branch .LBB0_1736
.Lp8fast:
	ds_read_b32 v190, v176 offset:704
	ds_read_b32 v188, v176 offset:640
	ds_read_b32 v186, v176 offset:576
	ds_read_b32 v184, v176 offset:512
	ds_read_b32 v182, v176 offset:192
	ds_read_b32 v180, v176 offset:128
	ds_read_b32 v178, v176 offset:64
	ds_read_b32 v176, v176
	s_lshl_b32 s22, s22, 7
	s_ashr_i32 s23, s22, 31
	s_mov_b32 s26, 0xbfb8aa3b
	v_mov_b64_e32 v[218:219], s[8:9]
	v_mad_u64_u32 v[218:219], s[24:25], v166, s53, v[218:219]
	v_mov_b32_e32 v220, v219
	v_mad_u64_u32 v[220:221], s[24:25], v167, s53, v[220:221]
	v_mov_b32_e32 v219, v220
	v_lshl_add_u64 v[218:219], s[22:23], 1, v[218:219]
	v_lshl_add_u64 v[218:219], v[218:219], 0, v[154:155]
	s_waitcnt vmcnt(0) lgkmcnt(0)
	v_pk_fma_f32 v[142:143], v[142:143], v[176:177], v[78:79] op_sel_hi:[1,0,1]
	v_pk_fma_f32 v[144:145], v[144:145], v[176:177], v[80:81] op_sel_hi:[1,0,1]
	v_pk_fma_f32 v[138:139], v[138:139], v[176:177], v[74:75] op_sel_hi:[1,0,1]
	v_pk_fma_f32 v[140:141], v[140:141], v[176:177], v[76:77] op_sel_hi:[1,0,1]
	v_pk_fma_f32 v[134:135], v[134:135], v[176:177], v[62:63] op_sel_hi:[1,0,1]
	v_pk_fma_f32 v[136:137], v[136:137], v[176:177], v[64:65] op_sel_hi:[1,0,1]
	v_pk_fma_f32 v[130:131], v[130:131], v[176:177], v[58:59] op_sel_hi:[1,0,1]
	v_pk_fma_f32 v[132:133], v[132:133], v[176:177], v[60:61] op_sel_hi:[1,0,1]
	v_pk_mul_f32 v[192:193], v[138:139], s[26:27] op_sel_hi:[1,0]
	v_pk_mul_f32 v[194:195], v[140:141], s[26:27] op_sel_hi:[1,0]
	v_pk_mul_f32 v[196:197], v[142:143], s[26:27] op_sel_hi:[1,0]
	v_pk_mul_f32 v[198:199], v[144:145], s[26:27] op_sel_hi:[1,0]
	v_exp_f32_e32 v192, v192
	v_exp_f32_e32 v193, v193
	v_exp_f32_e32 v194, v194
	v_exp_f32_e32 v195, v195
	v_exp_f32_e32 v196, v196
	v_exp_f32_e32 v197, v197
	v_exp_f32_e32 v198, v198
	v_exp_f32_e32 v199, v199
	v_add_f32_e32 v192, 1.0, v192
	v_add_f32_e32 v193, 1.0, v193
	v_add_f32_e32 v194, 1.0, v194
	v_add_f32_e32 v195, 1.0, v195
	v_add_f32_e32 v196, 1.0, v196
	v_add_f32_e32 v197, 1.0, v197
	v_add_f32_e32 v198, 1.0, v198
	v_add_f32_e32 v199, 1.0, v199
	v_rcp_f32_e32 v192, v192
	v_rcp_f32_e32 v193, v193
	v_rcp_f32_e32 v194, v194
	v_rcp_f32_e32 v195, v195
	v_rcp_f32_e32 v196, v196
	v_rcp_f32_e32 v197, v197
	v_rcp_f32_e32 v198, v198
	v_rcp_f32_e32 v199, v199
	v_pk_mul_f32 v[192:193], v[138:139], v[192:193]
	v_pk_mul_f32 v[194:195], v[140:141], v[194:195]
	v_pk_mul_f32 v[196:197], v[142:143], v[196:197]
	v_pk_mul_f32 v[198:199], v[144:145], v[198:199]
	v_pk_mul_f32 v[202:203], v[192:193], v[130:131]
	v_pk_mul_f32 v[204:205], v[194:195], v[132:133]
	v_pk_mul_f32 v[206:207], v[196:197], v[134:135]
	v_pk_mul_f32 v[208:209], v[198:199], v[136:137]
	v_cvt_pk_bf16_f32 v210, v206, v207
	v_cvt_pk_bf16_f32 v211, v208, v209
	v_cvt_pk_bf16_f32 v212, v202, v203
	v_cvt_pk_bf16_f32 v213, v204, v205
	global_store_dwordx4 v[218:219], v[210:213], off
	v_add_co_u32_e32 v218, vcc, 0x16000, v218
	s_nop 1
	v_addc_co_u32_e32 v219, vcc, 0, v219, vcc
	v_pk_fma_f32 v[126:127], v[126:127], v[178:179], v[78:79] op_sel_hi:[1,0,1]
	v_pk_fma_f32 v[128:129], v[128:129], v[178:179], v[80:81] op_sel_hi:[1,0,1]
	v_pk_fma_f32 v[122:123], v[122:123], v[178:179], v[74:75] op_sel_hi:[1,0,1]
	v_pk_fma_f32 v[124:125], v[124:125], v[178:179], v[76:77] op_sel_hi:[1,0,1]
	v_pk_fma_f32 v[118:119], v[118:119], v[178:179], v[62:63] op_sel_hi:[1,0,1]
	v_pk_fma_f32 v[120:121], v[120:121], v[178:179], v[64:65] op_sel_hi:[1,0,1]
	v_pk_fma_f32 v[114:115], v[114:115], v[178:179], v[58:59] op_sel_hi:[1,0,1]
	v_pk_fma_f32 v[116:117], v[116:117], v[178:179], v[60:61] op_sel_hi:[1,0,1]
	v_pk_mul_f32 v[192:193], v[122:123], s[26:27] op_sel_hi:[1,0]
	v_pk_mul_f32 v[194:195], v[124:125], s[26:27] op_sel_hi:[1,0]
	v_pk_mul_f32 v[196:197], v[126:127], s[26:27] op_sel_hi:[1,0]
	v_pk_mul_f32 v[198:199], v[128:129], s[26:27] op_sel_hi:[1,0]
	v_exp_f32_e32 v192, v192
	v_exp_f32_e32 v193, v193
	v_exp_f32_e32 v194, v194
	v_exp_f32_e32 v195, v195
	v_exp_f32_e32 v196, v196
	v_exp_f32_e32 v197, v197
	v_exp_f32_e32 v198, v198
	v_exp_f32_e32 v199, v199
	v_add_f32_e32 v192, 1.0, v192
	v_add_f32_e32 v193, 1.0, v193
	v_add_f32_e32 v194, 1.0, v194
	v_add_f32_e32 v195, 1.0, v195
	v_add_f32_e32 v196, 1.0, v196
	v_add_f32_e32 v197, 1.0, v197
	v_add_f32_e32 v198, 1.0, v198
	v_add_f32_e32 v199, 1.0, v199
	v_rcp_f32_e32 v192, v192
	v_rcp_f32_e32 v193, v193
	v_rcp_f32_e32 v194, v194
	v_rcp_f32_e32 v195, v195
	v_rcp_f32_e32 v196, v196
	v_rcp_f32_e32 v197, v197
	v_rcp_f32_e32 v198, v198
	v_rcp_f32_e32 v199, v199
	v_pk_mul_f32 v[192:193], v[122:123], v[192:193]
	v_pk_mul_f32 v[194:195], v[124:125], v[194:195]
	v_pk_mul_f32 v[196:197], v[126:127], v[196:197]
	v_pk_mul_f32 v[198:199], v[128:129], v[198:199]
	v_pk_mul_f32 v[202:203], v[192:193], v[114:115]
	v_pk_mul_f32 v[204:205], v[194:195], v[116:117]
	v_pk_mul_f32 v[206:207], v[196:197], v[118:119]
	v_pk_mul_f32 v[208:209], v[198:199], v[120:121]
	v_cvt_pk_bf16_f32 v210, v206, v207
	v_cvt_pk_bf16_f32 v211, v208, v209
	v_cvt_pk_bf16_f32 v212, v202, v203
	v_cvt_pk_bf16_f32 v213, v204, v205
	global_store_dwordx4 v[218:219], v[210:213], off
	v_add_co_u32_e32 v218, vcc, 0x16000, v218
	s_nop 1
	v_addc_co_u32_e32 v219, vcc, 0, v219, vcc
	v_pk_fma_f32 v[110:111], v[110:111], v[180:181], v[78:79] op_sel_hi:[1,0,1]
	v_pk_fma_f32 v[112:113], v[112:113], v[180:181], v[80:81] op_sel_hi:[1,0,1]
	v_pk_fma_f32 v[106:107], v[106:107], v[180:181], v[74:75] op_sel_hi:[1,0,1]
	v_pk_fma_f32 v[108:109], v[108:109], v[180:181], v[76:77] op_sel_hi:[1,0,1]
	v_pk_fma_f32 v[102:103], v[102:103], v[180:181], v[62:63] op_sel_hi:[1,0,1]
	v_pk_fma_f32 v[104:105], v[104:105], v[180:181], v[64:65] op_sel_hi:[1,0,1]
	v_pk_fma_f32 v[98:99], v[98:99], v[180:181], v[58:59] op_sel_hi:[1,0,1]
	v_pk_fma_f32 v[100:101], v[100:101], v[180:181], v[60:61] op_sel_hi:[1,0,1]
	v_pk_mul_f32 v[192:193], v[106:107], s[26:27] op_sel_hi:[1,0]
	v_pk_mul_f32 v[194:195], v[108:109], s[26:27] op_sel_hi:[1,0]
	v_pk_mul_f32 v[196:197], v[110:111], s[26:27] op_sel_hi:[1,0]
	v_pk_mul_f32 v[198:199], v[112:113], s[26:27] op_sel_hi:[1,0]
	v_exp_f32_e32 v192, v192
	v_exp_f32_e32 v193, v193
	v_exp_f32_e32 v194, v194
	v_exp_f32_e32 v195, v195
	v_exp_f32_e32 v196, v196
	v_exp_f32_e32 v197, v197
	v_exp_f32_e32 v198, v198
	v_exp_f32_e32 v199, v199
	v_add_f32_e32 v192, 1.0, v192
	v_add_f32_e32 v193, 1.0, v193
	v_add_f32_e32 v194, 1.0, v194
	v_add_f32_e32 v195, 1.0, v195
	v_add_f32_e32 v196, 1.0, v196
	v_add_f32_e32 v197, 1.0, v197
	v_add_f32_e32 v198, 1.0, v198
	v_add_f32_e32 v199, 1.0, v199
	v_rcp_f32_e32 v192, v192
	v_rcp_f32_e32 v193, v193
	v_rcp_f32_e32 v194, v194
	v_rcp_f32_e32 v195, v195
	v_rcp_f32_e32 v196, v196
	v_rcp_f32_e32 v197, v197
	v_rcp_f32_e32 v198, v198
	v_rcp_f32_e32 v199, v199
	v_pk_mul_f32 v[192:193], v[106:107], v[192:193]
	v_pk_mul_f32 v[194:195], v[108:109], v[194:195]
	v_pk_mul_f32 v[196:197], v[110:111], v[196:197]
	v_pk_mul_f32 v[198:199], v[112:113], v[198:199]
	v_pk_mul_f32 v[202:203], v[192:193], v[98:99]
	v_pk_mul_f32 v[204:205], v[194:195], v[100:101]
	v_pk_mul_f32 v[206:207], v[196:197], v[102:103]
	v_pk_mul_f32 v[208:209], v[198:199], v[104:105]
	v_cvt_pk_bf16_f32 v210, v206, v207
	v_cvt_pk_bf16_f32 v211, v208, v209
	v_cvt_pk_bf16_f32 v212, v202, v203
	v_cvt_pk_bf16_f32 v213, v204, v205
	global_store_dwordx4 v[218:219], v[210:213], off
	v_add_co_u32_e32 v218, vcc, 0x16000, v218
	s_nop 1
	v_addc_co_u32_e32 v219, vcc, 0, v219, vcc
	v_pk_fma_f32 v[94:95], v[94:95], v[182:183], v[78:79] op_sel_hi:[1,0,1]
	v_pk_fma_f32 v[96:97], v[96:97], v[182:183], v[80:81] op_sel_hi:[1,0,1]
	v_pk_fma_f32 v[90:91], v[90:91], v[182:183], v[74:75] op_sel_hi:[1,0,1]
	v_pk_fma_f32 v[92:93], v[92:93], v[182:183], v[76:77] op_sel_hi:[1,0,1]
	v_pk_fma_f32 v[86:87], v[86:87], v[182:183], v[62:63] op_sel_hi:[1,0,1]
	v_pk_fma_f32 v[88:89], v[88:89], v[182:183], v[64:65] op_sel_hi:[1,0,1]
	v_pk_fma_f32 v[82:83], v[82:83], v[182:183], v[58:59] op_sel_hi:[1,0,1]
	v_pk_fma_f32 v[84:85], v[84:85], v[182:183], v[60:61] op_sel_hi:[1,0,1]
	v_pk_mul_f32 v[192:193], v[90:91], s[26:27] op_sel_hi:[1,0]
	v_pk_mul_f32 v[194:195], v[92:93], s[26:27] op_sel_hi:[1,0]
	v_pk_mul_f32 v[196:197], v[94:95], s[26:27] op_sel_hi:[1,0]
	v_pk_mul_f32 v[198:199], v[96:97], s[26:27] op_sel_hi:[1,0]
	v_exp_f32_e32 v192, v192
	v_exp_f32_e32 v193, v193
	v_exp_f32_e32 v194, v194
	v_exp_f32_e32 v195, v195
	v_exp_f32_e32 v196, v196
	v_exp_f32_e32 v197, v197
	v_exp_f32_e32 v198, v198
	v_exp_f32_e32 v199, v199
	v_add_f32_e32 v192, 1.0, v192
	v_add_f32_e32 v193, 1.0, v193
	v_add_f32_e32 v194, 1.0, v194
	v_add_f32_e32 v195, 1.0, v195
	v_add_f32_e32 v196, 1.0, v196
	v_add_f32_e32 v197, 1.0, v197
	v_add_f32_e32 v198, 1.0, v198
	v_add_f32_e32 v199, 1.0, v199
	v_rcp_f32_e32 v192, v192
	v_rcp_f32_e32 v193, v193
	v_rcp_f32_e32 v194, v194
	v_rcp_f32_e32 v195, v195
	v_rcp_f32_e32 v196, v196
	v_rcp_f32_e32 v197, v197
	v_rcp_f32_e32 v198, v198
	v_rcp_f32_e32 v199, v199
	v_pk_mul_f32 v[192:193], v[90:91], v[192:193]
	v_pk_mul_f32 v[194:195], v[92:93], v[194:195]
	v_pk_mul_f32 v[196:197], v[94:95], v[196:197]
	v_pk_mul_f32 v[198:199], v[96:97], v[198:199]
	v_pk_mul_f32 v[202:203], v[192:193], v[82:83]
	v_pk_mul_f32 v[204:205], v[194:195], v[84:85]
	v_pk_mul_f32 v[206:207], v[196:197], v[86:87]
	v_pk_mul_f32 v[208:209], v[198:199], v[88:89]
	v_cvt_pk_bf16_f32 v210, v206, v207
	v_cvt_pk_bf16_f32 v211, v208, v209
	v_cvt_pk_bf16_f32 v212, v202, v203
	v_cvt_pk_bf16_f32 v213, v204, v205
	global_store_dwordx4 v[218:219], v[210:213], off
	v_add_co_u32_e32 v218, vcc, 0x6e000, v218
	s_nop 1
	v_addc_co_u32_e32 v219, vcc, 0, v219, vcc
	v_pk_fma_f32 v[70:71], v[70:71], v[184:185], v[78:79] op_sel_hi:[1,0,1]
	v_pk_fma_f32 v[72:73], v[72:73], v[184:185], v[80:81] op_sel_hi:[1,0,1]
	v_pk_fma_f32 v[66:67], v[66:67], v[184:185], v[74:75] op_sel_hi:[1,0,1]
	v_pk_fma_f32 v[68:69], v[68:69], v[184:185], v[76:77] op_sel_hi:[1,0,1]
	v_pk_fma_f32 v[54:55], v[54:55], v[184:185], v[62:63] op_sel_hi:[1,0,1]
	v_pk_fma_f32 v[56:57], v[56:57], v[184:185], v[64:65] op_sel_hi:[1,0,1]
	v_pk_fma_f32 v[50:51], v[50:51], v[184:185], v[58:59] op_sel_hi:[1,0,1]
	v_pk_fma_f32 v[52:53], v[52:53], v[184:185], v[60:61] op_sel_hi:[1,0,1]
	v_pk_mul_f32 v[192:193], v[66:67], s[26:27] op_sel_hi:[1,0]
	v_pk_mul_f32 v[194:195], v[68:69], s[26:27] op_sel_hi:[1,0]
	v_pk_mul_f32 v[196:197], v[70:71], s[26:27] op_sel_hi:[1,0]
	v_pk_mul_f32 v[198:199], v[72:73], s[26:27] op_sel_hi:[1,0]
	v_exp_f32_e32 v192, v192
	v_exp_f32_e32 v193, v193
	v_exp_f32_e32 v194, v194
	v_exp_f32_e32 v195, v195
	v_exp_f32_e32 v196, v196
	v_exp_f32_e32 v197, v197
	v_exp_f32_e32 v198, v198
	v_exp_f32_e32 v199, v199
	v_add_f32_e32 v192, 1.0, v192
	v_add_f32_e32 v193, 1.0, v193
	v_add_f32_e32 v194, 1.0, v194
	v_add_f32_e32 v195, 1.0, v195
	v_add_f32_e32 v196, 1.0, v196
	v_add_f32_e32 v197, 1.0, v197
	v_add_f32_e32 v198, 1.0, v198
	v_add_f32_e32 v199, 1.0, v199
	v_rcp_f32_e32 v192, v192
	v_rcp_f32_e32 v193, v193
	v_rcp_f32_e32 v194, v194
	v_rcp_f32_e32 v195, v195
	v_rcp_f32_e32 v196, v196
	v_rcp_f32_e32 v197, v197
	v_rcp_f32_e32 v198, v198
	v_rcp_f32_e32 v199, v199
	v_pk_mul_f32 v[192:193], v[66:67], v[192:193]
	v_pk_mul_f32 v[194:195], v[68:69], v[194:195]
	v_pk_mul_f32 v[196:197], v[70:71], v[196:197]
	v_pk_mul_f32 v[198:199], v[72:73], v[198:199]
	v_pk_mul_f32 v[202:203], v[192:193], v[50:51]
	v_pk_mul_f32 v[204:205], v[194:195], v[52:53]
	v_pk_mul_f32 v[206:207], v[196:197], v[54:55]
	v_pk_mul_f32 v[208:209], v[198:199], v[56:57]
	v_cvt_pk_bf16_f32 v210, v206, v207
	v_cvt_pk_bf16_f32 v211, v208, v209
	v_cvt_pk_bf16_f32 v212, v202, v203
	v_cvt_pk_bf16_f32 v213, v204, v205
	global_store_dwordx4 v[218:219], v[210:213], off
	v_add_co_u32_e32 v218, vcc, 0x16000, v218
	s_nop 1
	v_addc_co_u32_e32 v219, vcc, 0, v219, vcc
	v_pk_fma_f32 v[46:47], v[46:47], v[186:187], v[78:79] op_sel_hi:[1,0,1]
	v_pk_fma_f32 v[48:49], v[48:49], v[186:187], v[80:81] op_sel_hi:[1,0,1]
	v_pk_fma_f32 v[42:43], v[42:43], v[186:187], v[74:75] op_sel_hi:[1,0,1]
	v_pk_fma_f32 v[44:45], v[44:45], v[186:187], v[76:77] op_sel_hi:[1,0,1]
	v_pk_fma_f32 v[38:39], v[38:39], v[186:187], v[62:63] op_sel_hi:[1,0,1]
	v_pk_fma_f32 v[40:41], v[40:41], v[186:187], v[64:65] op_sel_hi:[1,0,1]
	v_pk_fma_f32 v[34:35], v[34:35], v[186:187], v[58:59] op_sel_hi:[1,0,1]
	v_pk_fma_f32 v[36:37], v[36:37], v[186:187], v[60:61] op_sel_hi:[1,0,1]
	v_pk_mul_f32 v[192:193], v[42:43], s[26:27] op_sel_hi:[1,0]
	v_pk_mul_f32 v[194:195], v[44:45], s[26:27] op_sel_hi:[1,0]
	v_pk_mul_f32 v[196:197], v[46:47], s[26:27] op_sel_hi:[1,0]
	v_pk_mul_f32 v[198:199], v[48:49], s[26:27] op_sel_hi:[1,0]
	v_exp_f32_e32 v192, v192
	v_exp_f32_e32 v193, v193
	v_exp_f32_e32 v194, v194
	v_exp_f32_e32 v195, v195
	v_exp_f32_e32 v196, v196
	v_exp_f32_e32 v197, v197
	v_exp_f32_e32 v198, v198
	v_exp_f32_e32 v199, v199
	v_add_f32_e32 v192, 1.0, v192
	v_add_f32_e32 v193, 1.0, v193
	v_add_f32_e32 v194, 1.0, v194
	v_add_f32_e32 v195, 1.0, v195
	v_add_f32_e32 v196, 1.0, v196
	v_add_f32_e32 v197, 1.0, v197
	v_add_f32_e32 v198, 1.0, v198
	v_add_f32_e32 v199, 1.0, v199
	v_rcp_f32_e32 v192, v192
	v_rcp_f32_e32 v193, v193
	v_rcp_f32_e32 v194, v194
	v_rcp_f32_e32 v195, v195
	v_rcp_f32_e32 v196, v196
	v_rcp_f32_e32 v197, v197
	v_rcp_f32_e32 v198, v198
	v_rcp_f32_e32 v199, v199
	v_pk_mul_f32 v[192:193], v[42:43], v[192:193]
	v_pk_mul_f32 v[194:195], v[44:45], v[194:195]
	v_pk_mul_f32 v[196:197], v[46:47], v[196:197]
	v_pk_mul_f32 v[198:199], v[48:49], v[198:199]
	v_pk_mul_f32 v[202:203], v[192:193], v[34:35]
	v_pk_mul_f32 v[204:205], v[194:195], v[36:37]
	v_pk_mul_f32 v[206:207], v[196:197], v[38:39]
	v_pk_mul_f32 v[208:209], v[198:199], v[40:41]
	v_cvt_pk_bf16_f32 v210, v206, v207
	v_cvt_pk_bf16_f32 v211, v208, v209
	v_cvt_pk_bf16_f32 v212, v202, v203
	v_cvt_pk_bf16_f32 v213, v204, v205
	global_store_dwordx4 v[218:219], v[210:213], off
	v_add_co_u32_e32 v218, vcc, 0x16000, v218
	s_nop 1
	v_addc_co_u32_e32 v219, vcc, 0, v219, vcc
	v_pk_fma_f32 v[30:31], v[30:31], v[188:189], v[78:79] op_sel_hi:[1,0,1]
	v_pk_fma_f32 v[32:33], v[32:33], v[188:189], v[80:81] op_sel_hi:[1,0,1]
	v_pk_fma_f32 v[26:27], v[26:27], v[188:189], v[74:75] op_sel_hi:[1,0,1]
	v_pk_fma_f32 v[28:29], v[28:29], v[188:189], v[76:77] op_sel_hi:[1,0,1]
	v_pk_fma_f32 v[22:23], v[22:23], v[188:189], v[62:63] op_sel_hi:[1,0,1]
	v_pk_fma_f32 v[24:25], v[24:25], v[188:189], v[64:65] op_sel_hi:[1,0,1]
	v_pk_fma_f32 v[18:19], v[18:19], v[188:189], v[58:59] op_sel_hi:[1,0,1]
	v_pk_fma_f32 v[20:21], v[20:21], v[188:189], v[60:61] op_sel_hi:[1,0,1]
	v_pk_mul_f32 v[192:193], v[26:27], s[26:27] op_sel_hi:[1,0]
	v_pk_mul_f32 v[194:195], v[28:29], s[26:27] op_sel_hi:[1,0]
	v_pk_mul_f32 v[196:197], v[30:31], s[26:27] op_sel_hi:[1,0]
	v_pk_mul_f32 v[198:199], v[32:33], s[26:27] op_sel_hi:[1,0]
	v_exp_f32_e32 v192, v192
	v_exp_f32_e32 v193, v193
	v_exp_f32_e32 v194, v194
	v_exp_f32_e32 v195, v195
	v_exp_f32_e32 v196, v196
	v_exp_f32_e32 v197, v197
	v_exp_f32_e32 v198, v198
	v_exp_f32_e32 v199, v199
	v_add_f32_e32 v192, 1.0, v192
	v_add_f32_e32 v193, 1.0, v193
	v_add_f32_e32 v194, 1.0, v194
	v_add_f32_e32 v195, 1.0, v195
	v_add_f32_e32 v196, 1.0, v196
	v_add_f32_e32 v197, 1.0, v197
	v_add_f32_e32 v198, 1.0, v198
	v_add_f32_e32 v199, 1.0, v199
	v_rcp_f32_e32 v192, v192
	v_rcp_f32_e32 v193, v193
	v_rcp_f32_e32 v194, v194
	v_rcp_f32_e32 v195, v195
	v_rcp_f32_e32 v196, v196
	v_rcp_f32_e32 v197, v197
	v_rcp_f32_e32 v198, v198
	v_rcp_f32_e32 v199, v199
	v_pk_mul_f32 v[192:193], v[26:27], v[192:193]
	v_pk_mul_f32 v[194:195], v[28:29], v[194:195]
	v_pk_mul_f32 v[196:197], v[30:31], v[196:197]
	v_pk_mul_f32 v[198:199], v[32:33], v[198:199]
	v_pk_mul_f32 v[202:203], v[192:193], v[18:19]
	v_pk_mul_f32 v[204:205], v[194:195], v[20:21]
	v_pk_mul_f32 v[206:207], v[196:197], v[22:23]
	v_pk_mul_f32 v[208:209], v[198:199], v[24:25]
	v_cvt_pk_bf16_f32 v210, v206, v207
	v_cvt_pk_bf16_f32 v211, v208, v209
	v_cvt_pk_bf16_f32 v212, v202, v203
	v_cvt_pk_bf16_f32 v213, v204, v205
	global_store_dwordx4 v[218:219], v[210:213], off
	v_add_co_u32_e32 v218, vcc, 0x16000, v218
	s_nop 1
	v_addc_co_u32_e32 v219, vcc, 0, v219, vcc
	v_pk_fma_f32 v[14:15], v[14:15], v[190:191], v[78:79] op_sel_hi:[1,0,1]
	v_pk_fma_f32 v[16:17], v[16:17], v[190:191], v[80:81] op_sel_hi:[1,0,1]
	v_pk_fma_f32 v[10:11], v[10:11], v[190:191], v[74:75] op_sel_hi:[1,0,1]
	v_pk_fma_f32 v[12:13], v[12:13], v[190:191], v[76:77] op_sel_hi:[1,0,1]
	v_pk_fma_f32 v[6:7], v[6:7], v[190:191], v[62:63] op_sel_hi:[1,0,1]
	v_pk_fma_f32 v[8:9], v[8:9], v[190:191], v[64:65] op_sel_hi:[1,0,1]
	v_pk_fma_f32 v[2:3], v[2:3], v[190:191], v[58:59] op_sel_hi:[1,0,1]
	v_pk_fma_f32 v[4:5], v[4:5], v[190:191], v[60:61] op_sel_hi:[1,0,1]
	v_pk_mul_f32 v[192:193], v[10:11], s[26:27] op_sel_hi:[1,0]
	v_pk_mul_f32 v[194:195], v[12:13], s[26:27] op_sel_hi:[1,0]
	v_pk_mul_f32 v[196:197], v[14:15], s[26:27] op_sel_hi:[1,0]
	v_pk_mul_f32 v[198:199], v[16:17], s[26:27] op_sel_hi:[1,0]
	v_exp_f32_e32 v192, v192
	v_exp_f32_e32 v193, v193
	v_exp_f32_e32 v194, v194
	v_exp_f32_e32 v195, v195
	v_exp_f32_e32 v196, v196
	v_exp_f32_e32 v197, v197
	v_exp_f32_e32 v198, v198
	v_exp_f32_e32 v199, v199
	v_add_f32_e32 v192, 1.0, v192
	v_add_f32_e32 v193, 1.0, v193
	v_add_f32_e32 v194, 1.0, v194
	v_add_f32_e32 v195, 1.0, v195
	v_add_f32_e32 v196, 1.0, v196
	v_add_f32_e32 v197, 1.0, v197
	v_add_f32_e32 v198, 1.0, v198
	v_add_f32_e32 v199, 1.0, v199
	v_rcp_f32_e32 v192, v192
	v_rcp_f32_e32 v193, v193
	v_rcp_f32_e32 v194, v194
	v_rcp_f32_e32 v195, v195
	v_rcp_f32_e32 v196, v196
	v_rcp_f32_e32 v197, v197
	v_rcp_f32_e32 v198, v198
	v_rcp_f32_e32 v199, v199
	v_pk_mul_f32 v[192:193], v[10:11], v[192:193]
	v_pk_mul_f32 v[194:195], v[12:13], v[194:195]
	v_pk_mul_f32 v[196:197], v[14:15], v[196:197]
	v_pk_mul_f32 v[198:199], v[16:17], v[198:199]
	v_pk_mul_f32 v[202:203], v[192:193], v[2:3]
	v_pk_mul_f32 v[204:205], v[194:195], v[4:5]
	v_pk_mul_f32 v[206:207], v[196:197], v[6:7]
	v_pk_mul_f32 v[208:209], v[198:199], v[8:9]
	v_cvt_pk_bf16_f32 v210, v206, v207
	v_cvt_pk_bf16_f32 v211, v208, v209
	v_cvt_pk_bf16_f32 v212, v202, v203
	v_cvt_pk_bf16_f32 v213, v204, v205
	global_store_dwordx4 v[218:219], v[210:213], off
	s_andn2_b64 vcc, exec, s[4:5]
	s_mov_b64 s[4:5], -1
	s_branch .Lp8_tail
